# v23 + P0 expert stores deferred past the next load burst (in-order vmcnt no longer waits on fresh write-through store acks)
# baseline (speedup 1.0000x reference)
; #define MOE_LOAD(v, it) do { _Pragma("unroll") for (int i_ = 0; i_ < 64; ++i_) v[i_] = __builtin_nontemporal_load((it).src + (size_t)(2 * i_) * (it).stride); } while (0)
;     ...
;         for (int j = 0; j < nmine; j += 2) {
;             const int it1 = gw + (j + 1) * NGW, it2 = gw + (j + 2) * NGW;
;             ib = moe_item(wg, wu, wd, win, wout, wpn, wpd, F.ws, it1 <= last ? it1 : last, F.lane); MOE_LOAD(vb, ib);
;             MOE_PROC(va, ia);
;             ia = moe_item(wg, wu, wd, win, wout, wpn, wpd, F.ws, it2 <= last ? it2 : last, F.lane); MOE_LOAD(va, ia);
;             MOE_PROC(vb, ib);
;         }
.LBB0_80:
	s_lshl_b64 s[68:69], s[68:69], 3
	v_lshl_add_u64 v[14:15], v[16:17], 0, s[68:69]
	global_load_dword v87, v[16:17], off nt
	v_lshl_add_u64 v[16:17], v[14:15], 0, s[68:69]
	v_lshl_add_u64 v[30:31], v[16:17], 0, s[68:69]
	v_lshl_add_u64 v[32:33], v[30:31], 0, s[68:69]
	v_lshl_add_u64 v[34:35], v[32:33], 0, s[68:69]
	v_lshl_add_u64 v[36:37], v[34:35], 0, s[68:69]
	v_lshl_add_u64 v[38:39], v[36:37], 0, s[68:69]
	v_lshl_add_u64 v[40:41], v[38:39], 0, s[68:69]
	global_load_dword v92, v[14:15], off nt
	global_load_dword v91, v[16:17], off nt
	global_load_dword v90, v[30:31], off nt
	global_load_dword v89, v[32:33], off nt
	global_load_dword v88, v[34:35], off nt
	global_load_dword v86, v[36:37], off nt
	global_load_dword v85, v[38:39], off nt
	global_load_dword v83, v[40:41], off nt
	v_lshl_add_u64 v[14:15], v[40:41], 0, s[68:69]
	v_lshl_add_u64 v[16:17], v[14:15], 0, s[68:69]
	global_load_dword v84, v[14:15], off nt
	global_load_dword v79, v[16:17], off nt
	v_lshl_add_u64 v[14:15], v[16:17], 0, s[68:69]
	global_load_dword v80, v[14:15], off nt
	v_lshl_add_u64 v[14:15], v[14:15], 0, s[68:69]
	global_load_dword v75, v[14:15], off nt
	v_lshl_add_u64 v[14:15], v[14:15], 0, s[68:69]
	global_load_dword v76, v[14:15], off nt
	v_lshl_add_u64 v[14:15], v[14:15], 0, s[68:69]
	global_load_dword v71, v[14:15], off nt
	v_lshl_add_u64 v[14:15], v[14:15], 0, s[68:69]
	global_load_dword v72, v[14:15], off nt
	v_lshl_add_u64 v[14:15], v[14:15], 0, s[68:69]
	global_load_dword v65, v[14:15], off nt
	v_lshl_add_u64 v[14:15], v[14:15], 0, s[68:69]
	global_load_dword v66, v[14:15], off nt
	v_lshl_add_u64 v[14:15], v[14:15], 0, s[68:69]
	global_load_dword v61, v[14:15], off nt
	v_lshl_add_u64 v[14:15], v[14:15], 0, s[68:69]
	global_load_dword v62, v[14:15], off nt
	v_lshl_add_u64 v[14:15], v[14:15], 0, s[68:69]
	global_load_dword v57, v[14:15], off nt
	v_lshl_add_u64 v[14:15], v[14:15], 0, s[68:69]
	global_load_dword v58, v[14:15], off nt
	v_lshl_add_u64 v[14:15], v[14:15], 0, s[68:69]
	global_load_dword v53, v[14:15], off nt
	v_lshl_add_u64 v[14:15], v[14:15], 0, s[68:69]
	global_load_dword v54, v[14:15], off nt
	v_lshl_add_u64 v[14:15], v[14:15], 0, s[68:69]
	global_load_dword v45, v[14:15], off nt
	v_lshl_add_u64 v[14:15], v[14:15], 0, s[68:69]
	global_load_dword v46, v[14:15], off nt
	v_lshl_add_u64 v[14:15], v[14:15], 0, s[68:69]
	global_load_dword v35, v[14:15], off nt
	v_lshl_add_u64 v[14:15], v[14:15], 0, s[68:69]
	global_load_dword v36, v[14:15], off nt
	v_lshl_add_u64 v[14:15], v[14:15], 0, s[68:69]
	global_load_dword v33, v[14:15], off nt
	v_lshl_add_u64 v[14:15], v[14:15], 0, s[68:69]
	global_load_dword v34, v[14:15], off nt
	v_lshl_add_u64 v[14:15], v[14:15], 0, s[68:69]
	global_load_dword v31, v[14:15], off nt
	v_lshl_add_u64 v[14:15], v[14:15], 0, s[68:69]
	global_load_dword v32, v[14:15], off nt
	v_lshl_add_u64 v[14:15], v[14:15], 0, s[68:69]
	global_load_dword v29, v[14:15], off nt
	v_lshl_add_u64 v[14:15], v[14:15], 0, s[68:69]
	global_load_dword v30, v[14:15], off nt
	v_lshl_add_u64 v[14:15], v[14:15], 0, s[68:69]
	global_load_dword v81, v[14:15], off nt
	v_lshl_add_u64 v[14:15], v[14:15], 0, s[68:69]
	global_load_dword v82, v[14:15], off nt
	v_lshl_add_u64 v[14:15], v[14:15], 0, s[68:69]
	global_load_dword v77, v[14:15], off nt
	v_lshl_add_u64 v[14:15], v[14:15], 0, s[68:69]
	global_load_dword v78, v[14:15], off nt
	v_lshl_add_u64 v[14:15], v[14:15], 0, s[68:69]
	global_load_dword v73, v[14:15], off nt
	v_lshl_add_u64 v[14:15], v[14:15], 0, s[68:69]
	global_load_dword v74, v[14:15], off nt
	v_lshl_add_u64 v[14:15], v[14:15], 0, s[68:69]
	global_load_dword v69, v[14:15], off nt
	v_lshl_add_u64 v[14:15], v[14:15], 0, s[68:69]
	global_load_dword v70, v[14:15], off nt
	v_lshl_add_u64 v[14:15], v[14:15], 0, s[68:69]
	global_load_dword v67, v[14:15], off nt
	v_lshl_add_u64 v[14:15], v[14:15], 0, s[68:69]
	global_load_dword v68, v[14:15], off nt
	v_lshl_add_u64 v[14:15], v[14:15], 0, s[68:69]
	global_load_dword v63, v[14:15], off nt
	v_lshl_add_u64 v[14:15], v[14:15], 0, s[68:69]
	global_load_dword v64, v[14:15], off nt
	v_lshl_add_u64 v[14:15], v[14:15], 0, s[68:69]
	global_load_dword v59, v[14:15], off nt
	v_lshl_add_u64 v[14:15], v[14:15], 0, s[68:69]
	global_load_dword v60, v[14:15], off nt
	v_lshl_add_u64 v[14:15], v[14:15], 0, s[68:69]
	global_load_dword v55, v[14:15], off nt
	v_lshl_add_u64 v[14:15], v[14:15], 0, s[68:69]
	global_load_dword v56, v[14:15], off nt
	v_lshl_add_u64 v[14:15], v[14:15], 0, s[68:69]
	global_load_dword v51, v[14:15], off nt
	v_lshl_add_u64 v[14:15], v[14:15], 0, s[68:69]
	global_load_dword v52, v[14:15], off nt
	v_lshl_add_u64 v[14:15], v[14:15], 0, s[68:69]
	global_load_dword v38, v[14:15], off nt
	v_lshl_add_u64 v[14:15], v[14:15], 0, s[68:69]
	global_load_dword v39, v[14:15], off nt
	v_lshl_add_u64 v[14:15], v[14:15], 0, s[68:69]
	global_load_dword v40, v[14:15], off nt
	v_lshl_add_u64 v[14:15], v[14:15], 0, s[68:69]
	global_load_dword v42, v[14:15], off nt
	v_lshl_add_u64 v[14:15], v[14:15], 0, s[68:69]
	global_load_dword v37, v[14:15], off nt
	v_lshl_add_u64 v[14:15], v[14:15], 0, s[68:69]
	global_load_dword v41, v[14:15], off nt
	v_lshl_add_u64 v[14:15], v[14:15], 0, s[68:69]
	global_load_dword v43, v[14:15], off nt
	v_lshl_add_u64 v[14:15], v[14:15], 0, s[68:69]
	global_load_dword v44, v[14:15], off nt
	v_lshl_add_u64 v[14:15], v[14:15], 0, s[68:69]
	global_load_dword v47, v[14:15], off nt
	v_lshl_add_u64 v[14:15], v[14:15], 0, s[68:69]
	global_load_dword v48, v[14:15], off nt
	v_lshl_add_u64 v[14:15], v[14:15], 0, s[68:69]
	global_load_dword v49, v[14:15], off nt
	v_lshl_add_u64 v[14:15], v[14:15], 0, s[68:69]
	global_store_dwordx4 v[196:197], v[204:207], off sc0 sc1 nt
	global_store_dwordx4 v[198:199], v[208:211], off sc0 sc1 nt
	global_store_dwordx4 v[200:201], v[212:215], off sc0 sc1 nt
	global_store_dwordx4 v[202:203], v[216:219], off sc0 sc1 nt
	s_waitcnt vmcnt(63)
	ds_write2st64_b32 v28, v93, v101 offset1:1
	ds_write2st64_b32 v28, v99, v100 offset0:2 offset1:3
	ds_write2st64_b32 v28, v97, v98 offset0:4 offset1:5
	ds_write2st64_b32 v28, v95, v96 offset0:6 offset1:7
	ds_write2st64_b32 v21, v94, v124 offset0:8 offset1:9
	ds_write2st64_b32 v21, v104, v114 offset0:10 offset1:11
	ds_write2st64_b32 v21, v105, v115 offset0:12 offset1:13
	ds_write2st64_b32 v21, v106, v116 offset0:14 offset1:15
	ds_write2st64_b32 v22, v107, v117 offset0:16 offset1:17
	ds_write2st64_b32 v22, v108, v118 offset0:18 offset1:19
	ds_write2st64_b32 v22, v109, v119 offset0:20 offset1:21
	ds_write2st64_b32 v22, v110, v120 offset0:22 offset1:23
	ds_write2st64_b32 v23, v111, v121 offset0:24 offset1:25
	ds_write2st64_b32 v23, v112, v122 offset0:26 offset1:27
	global_load_dword v50, v[14:15], off nt
	ds_write2st64_b32 v23, v102, v103 offset0:28 offset1:29
	ds_write2st64_b32 v23, v113, v123 offset0:30 offset1:31
	ds_write2st64_b32 v24, v125, v126 offset0:32 offset1:33
	ds_write2st64_b32 v24, v127, v128 offset0:34 offset1:35
	ds_write2st64_b32 v24, v129, v130 offset0:36 offset1:37
	ds_write2st64_b32 v24, v131, v132 offset0:38 offset1:39
	ds_write2st64_b32 v25, v133, v134 offset0:40 offset1:41
	ds_write2st64_b32 v25, v135, v136 offset0:42 offset1:43
	ds_write2st64_b32 v25, v137, v138 offset0:44 offset1:45
	ds_write2st64_b32 v25, v139, v140 offset0:46 offset1:47
	ds_write2st64_b32 v26, v141, v142 offset0:48 offset1:49
	ds_write2st64_b32 v26, v143, v144 offset0:50 offset1:51
	ds_write2st64_b32 v26, v146, v147 offset0:52 offset1:53
	ds_write2st64_b32 v26, v148, v149 offset0:54 offset1:55
	ds_write2st64_b32 v27, v151, v152 offset0:56 offset1:57
	ds_write2st64_b32 v27, v153, v154 offset0:58 offset1:59
	ds_write2st64_b32 v27, v155, v157 offset0:60 offset1:61
	ds_write2st64_b32 v27, v158, v159 offset0:62 offset1:63
	s_waitcnt lgkmcnt(0)
	ds_read2_b32 v[16:17], v1 offset1:32
	v_lshlrev_b64 v[14:15], s44, v[2:3]
	v_lshl_add_u64 v[12:13], v[12:13], 0, v[14:15]
	v_lshl_add_u64 v[98:99], v[12:13], 0, v[6:7]
	v_mov_b32_e32 v12, 0
	s_waitcnt lgkmcnt(0)
	v_mul_f32_e32 v4, 0x42800000, v16
	v_mul_f32_e32 v13, 0x42800000, v17
	ds_read2_b32 v[16:17], v1 offset0:64 offset1:96
	ds_read2_b32 v[94:95], v1 offset0:128 offset1:160
	v_cvt_pk_fp8_f32 v12, v4, v13
	v_lshlrev_b64 v[14:15], s46, v[2:3]
	v_lshl_add_u64 v[10:11], v[10:11], 0, v[14:15]
	s_waitcnt lgkmcnt(1)
	v_mul_f32_e32 v4, 0x42800000, v16
	v_mul_f32_e32 v13, 0x42800000, v17
	v_cvt_pk_fp8_f32 v12, v4, v13 op_sel:[0,0,1]
	s_waitcnt lgkmcnt(0)
	v_mul_f32_e32 v4, 0x42800000, v94
	ds_read2_b32 v[14:15], v1 offset0:192 offset1:224
	v_mul_f32_e32 v16, 0x42800000, v95
	v_mov_b32_e32 v13, 0
	v_cvt_pk_fp8_f32 v13, v4, v16
	ds_read2_b32 v[16:17], v145 offset1:32
	s_waitcnt lgkmcnt(1)
	v_mul_f32_e32 v4, 0x42800000, v14
	v_mul_f32_e32 v93, 0x42800000, v15
	ds_read2_b32 v[14:15], v145 offset0:64 offset1:96
	v_cvt_pk_fp8_f32 v13, v4, v93 op_sel:[0,0,1]
	s_waitcnt lgkmcnt(1)
	v_mul_f32_e32 v4, 0x42800000, v16
	v_mul_f32_e32 v93, 0x42800000, v17
	ds_read2_b32 v[16:17], v145 offset0:128 offset1:160
	s_waitcnt lgkmcnt(1)
	v_mul_f32_e32 v96, 0x42800000, v14
	v_mov_b32_e32 v14, 0
	v_cvt_pk_fp8_f32 v14, v4, v93
	v_mul_f32_e32 v97, 0x42800000, v15
	s_waitcnt lgkmcnt(0)
	v_mul_f32_e32 v4, 0x42800000, v16
	v_mul_f32_e32 v93, 0x42800000, v17
	ds_read2_b32 v[16:17], v145 offset0:192 offset1:224
	v_mov_b32_e32 v15, 0
	v_cvt_pk_fp8_f32 v15, v4, v93
	ds_read2_b32 v[94:95], v9 offset1:32
	v_cvt_pk_fp8_f32 v14, v96, v97 op_sel:[0,0,1]
	s_waitcnt lgkmcnt(1)
	v_mul_f32_e32 v4, 0x42800000, v16
	v_mul_f32_e32 v16, 0x42800000, v17
	v_cvt_pk_fp8_f32 v15, v4, v16 op_sel:[0,0,1]
	ds_read2_b32 v[16:17], v9 offset0:64 offset1:96
	s_waitcnt lgkmcnt(1)
	v_mul_f32_e32 v4, 0x42800000, v94
	v_mul_f32_e32 v93, 0x42800000, v95
	v_mov_b32_e32 v94, 0
	ds_read2_b32 v[96:97], v9 offset0:128 offset1:160
	v_cvt_pk_fp8_f32 v94, v4, v93
	s_nop 0
	v_mov_b64_e32 v[172:173], v[98:99]
	v_mov_b64_e32 v[180:181], v[12:13]
	v_mov_b64_e32 v[182:183], v[14:15]
	s_waitcnt lgkmcnt(1)
	v_mul_f32_e32 v4, 0x42800000, v16
	v_mov_b32_e32 v95, 0
	v_mul_f32_e32 v12, 0x42800000, v17
	v_cvt_pk_fp8_f32 v94, v4, v12 op_sel:[0,0,1]
	s_waitcnt lgkmcnt(0)
	v_mul_f32_e32 v4, 0x42800000, v96
	ds_read2_b32 v[12:13], v9 offset0:192 offset1:224
	v_mul_f32_e32 v14, 0x42800000, v97
	v_cvt_pk_fp8_f32 v95, v4, v14
	ds_read2_b32 v[14:15], v150 offset1:32
	v_mov_b32_e32 v96, 0
	s_waitcnt lgkmcnt(1)
	v_mul_f32_e32 v4, 0x42800000, v12
	v_mul_f32_e32 v16, 0x42800000, v13
	ds_read2_b32 v[12:13], v150 offset0:64 offset1:96
	v_cvt_pk_fp8_f32 v95, v4, v16 op_sel:[0,0,1]
	s_waitcnt lgkmcnt(1)
	v_mul_f32_e32 v4, 0x42800000, v14
	v_mul_f32_e32 v16, 0x42800000, v15
	ds_read2_b32 v[14:15], v150 offset0:128 offset1:160
	s_waitcnt lgkmcnt(1)
	v_mul_f32_e32 v17, 0x42800000, v12
	v_mul_f32_e32 v93, 0x42800000, v13
	ds_read2_b32 v[12:13], v150 offset0:192 offset1:224
	v_cvt_pk_fp8_f32 v96, v4, v16
	s_waitcnt lgkmcnt(1)
	v_mul_f32_e32 v4, 0x42800000, v14
	v_mul_f32_e32 v14, 0x42800000, v15
	v_mov_b32_e32 v97, 0
	v_cvt_pk_fp8_f32 v97, v4, v14
	s_waitcnt lgkmcnt(0)
	v_mul_f32_e32 v4, 0x42800000, v12
	v_mul_f32_e32 v12, 0x42800000, v13
	v_cvt_pk_fp8_f32 v96, v17, v93 op_sel:[0,0,1]
	v_cvt_pk_fp8_f32 v97, v4, v12 op_sel:[0,0,1]
	s_lshl_b32 s4, s42, 3
	ds_read2_b32 v[12:13], v18 offset1:32
	v_lshl_add_u64 v[16:17], v[98:99], 0, s[4:5]
	ds_read2_b32 v[14:15], v18 offset0:64 offset1:96
	s_nop 0
	v_mov_b64_e32 v[174:175], v[16:17]
	v_mov_b64_e32 v[184:185], v[94:95]
	v_mov_b64_e32 v[186:187], v[96:97]
	ds_read2_b32 v[94:95], v18 offset0:128 offset1:160
	s_waitcnt lgkmcnt(2)
	v_mul_f32_e32 v4, 0x42800000, v12
	v_mul_f32_e32 v13, 0x42800000, v13
	v_mov_b32_e32 v12, 0
	s_waitcnt lgkmcnt(1)
	v_mul_f32_e32 v93, 0x42800000, v14
	v_mul_f32_e32 v96, 0x42800000, v15
	v_cvt_pk_fp8_f32 v12, v4, v13
	s_waitcnt lgkmcnt(0)
	v_mul_f32_e32 v4, 0x42800000, v94
	v_mul_f32_e32 v94, 0x42800000, v95
	ds_read2_b32 v[14:15], v18 offset0:192 offset1:224
	v_mov_b32_e32 v13, 0
	v_cvt_pk_fp8_f32 v13, v4, v94
	ds_read2_b32 v[94:95], v156 offset1:32
	v_cvt_pk_fp8_f32 v12, v93, v96 op_sel:[0,0,1]
	s_waitcnt lgkmcnt(1)
	v_mul_f32_e32 v4, 0x42800000, v14
	v_mul_f32_e32 v14, 0x42800000, v15
	ds_read2_b32 v[96:97], v156 offset0:64 offset1:96
	v_cvt_pk_fp8_f32 v13, v4, v14 op_sel:[0,0,1]
	s_waitcnt lgkmcnt(1)
	v_mul_f32_e32 v4, 0x42800000, v94
	v_mul_f32_e32 v15, 0x42800000, v95
	v_mov_b32_e32 v14, 0
	ds_read2_b32 v[94:95], v156 offset0:128 offset1:160
	v_cvt_pk_fp8_f32 v14, v4, v15
	s_waitcnt lgkmcnt(1)
	v_mul_f32_e32 v4, 0x42800000, v96
	v_mul_f32_e32 v15, 0x42800000, v97
	ds_read2_b32 v[96:97], v156 offset0:192 offset1:224
	v_cvt_pk_fp8_f32 v14, v4, v15 op_sel:[0,0,1]
	s_waitcnt lgkmcnt(1)
	v_mul_f32_e32 v4, 0x42800000, v94
	v_mul_f32_e32 v93, 0x42800000, v95
	ds_read2_b32 v[94:95], v19 offset1:32
	s_waitcnt lgkmcnt(1)
	v_mul_f32_e32 v100, 0x42800000, v96
	v_mul_f32_e32 v101, 0x42800000, v97
	v_mov_b32_e32 v15, 0
	ds_read2_b32 v[96:97], v19 offset0:64 offset1:96
	v_cvt_pk_fp8_f32 v15, v4, v93
	s_waitcnt lgkmcnt(1)
	v_mul_f32_e32 v4, 0x42800000, v94
	v_mul_f32_e32 v93, 0x42800000, v95
	v_mov_b32_e32 v94, 0
	ds_read2_b32 v[98:99], v19 offset0:128 offset1:160
	v_cvt_pk_fp8_f32 v94, v4, v93
	s_waitcnt lgkmcnt(1)
	v_mul_f32_e32 v4, 0x42800000, v96
	v_mul_f32_e32 v93, 0x42800000, v97
	ds_read2_b32 v[96:97], v19 offset0:192 offset1:224
	v_cvt_pk_fp8_f32 v94, v4, v93 op_sel:[0,0,1]
	s_waitcnt lgkmcnt(1)
	v_mul_f32_e32 v4, 0x42800000, v98
	v_mul_f32_e32 v93, 0x42800000, v99
	v_mov_b32_e32 v95, 0
	ds_read2_b32 v[98:99], v160 offset1:32
	v_cvt_pk_fp8_f32 v95, v4, v93
	s_waitcnt lgkmcnt(1)
	v_mul_f32_e32 v4, 0x42800000, v96
	v_mul_f32_e32 v93, 0x42800000, v97
	ds_read2_b32 v[96:97], v160 offset0:64 offset1:96
	v_cvt_pk_fp8_f32 v95, v4, v93 op_sel:[0,0,1]
	s_waitcnt lgkmcnt(1)
	v_mul_f32_e32 v4, 0x42800000, v98
	v_mul_f32_e32 v93, 0x42800000, v99
	ds_read2_b32 v[98:99], v160 offset0:128 offset1:160
	v_cvt_pk_fp8_f32 v15, v100, v101 op_sel:[0,0,1]
	s_waitcnt lgkmcnt(1)
	v_mul_f32_e32 v102, 0x42800000, v96
	v_mov_b32_e32 v96, 0
	ds_read2_b32 v[100:101], v160 offset0:192 offset1:224
	v_mul_f32_e32 v103, 0x42800000, v97
	v_cvt_pk_fp8_f32 v96, v4, v93
	s_waitcnt lgkmcnt(1)
	v_mul_f32_e32 v4, 0x42800000, v98
	v_mul_f32_e32 v93, 0x42800000, v99
	v_mov_b32_e32 v97, 0
	v_cvt_pk_fp8_f32 v97, v4, v93
	s_waitcnt lgkmcnt(0)
	v_mul_f32_e32 v4, 0x42800000, v100
	v_mul_f32_e32 v93, 0x42800000, v101
	v_cvt_pk_fp8_f32 v96, v102, v103 op_sel:[0,0,1]
	v_cvt_pk_fp8_f32 v97, v4, v93 op_sel:[0,0,1]
	v_lshl_add_u64 v[16:17], v[16:17], 0, s[4:5]
	s_nop 0
	v_mov_b64_e32 v[176:177], v[16:17]
	v_mov_b64_e32 v[188:189], v[12:13]
	v_mov_b64_e32 v[190:191], v[14:15]
	s_add_i32 s91, s91, 2
	s_cmp_ge_i32 s91, s6
	v_lshl_add_u64 v[12:13], v[16:17], 0, s[4:5]
	s_nop 0
	v_mov_b64_e32 v[178:179], v[12:13]
	v_mov_b64_e32 v[192:193], v[94:95]
	v_mov_b64_e32 v[194:195], v[96:97]
	s_waitcnt lgkmcnt(0)
	s_mov_b64 s[100:101], -1
	s_cbranch_scc1 .LBB0_130

; #define MOE_LOAD(v, it) do { _Pragma("unroll") for (int i_ = 0; i_ < 64; ++i_) v[i_] = __builtin_nontemporal_load((it).src + (size_t)(2 * i_) * (it).stride); } while (0)
;     ...
;         for (int j = 0; j < nmine; j += 2) {
;             const int it1 = gw + (j + 1) * NGW, it2 = gw + (j + 2) * NGW;
;             ib = moe_item(wg, wu, wd, win, wout, wpn, wpd, F.ws, it1 <= last ? it1 : last, F.lane); MOE_LOAD(vb, ib);
;             MOE_PROC(va, ia);
;             ia = moe_item(wg, wu, wd, win, wout, wpn, wpd, F.ws, it2 <= last ? it2 : last, F.lane); MOE_LOAD(va, ia);
;             MOE_PROC(vb, ib);
;         }
.LBB0_105:
	s_lshl_b64 s[46:47], s[46:47], 3
	global_load_dword v93, v[16:17], off nt
	v_lshl_add_u64 v[16:17], v[16:17], 0, s[46:47]
	v_lshl_add_u64 v[94:95], v[16:17], 0, s[46:47]
	v_lshl_add_u64 v[96:97], v[94:95], 0, s[46:47]
	v_lshl_add_u64 v[102:103], v[96:97], 0, s[46:47]
	v_lshl_add_u64 v[104:105], v[102:103], 0, s[46:47]
	v_lshl_add_u64 v[106:107], v[104:105], 0, s[46:47]
	v_lshl_add_u64 v[108:109], v[106:107], 0, s[46:47]
	v_lshl_add_u64 v[110:111], v[108:109], 0, s[46:47]
	global_load_dword v101, v[16:17], off nt
	global_load_dword v99, v[94:95], off nt
	global_load_dword v100, v[96:97], off nt
	s_nop 0
	global_load_dword v97, v[102:103], off nt
	global_load_dword v98, v[104:105], off nt
	global_load_dword v95, v[106:107], off nt
	global_load_dword v96, v[108:109], off nt
	global_load_dword v94, v[110:111], off nt
	v_lshl_add_u64 v[16:17], v[110:111], 0, s[46:47]
	v_lshl_add_u64 v[102:103], v[16:17], 0, s[46:47]
	global_load_dword v124, v[16:17], off nt
	global_load_dword v104, v[102:103], off nt
	v_lshl_add_u64 v[16:17], v[102:103], 0, s[46:47]
	global_load_dword v114, v[16:17], off nt
	v_lshl_add_u64 v[16:17], v[16:17], 0, s[46:47]
	global_load_dword v105, v[16:17], off nt
	v_lshl_add_u64 v[16:17], v[16:17], 0, s[46:47]
	global_load_dword v115, v[16:17], off nt
	v_lshl_add_u64 v[16:17], v[16:17], 0, s[46:47]
	global_load_dword v106, v[16:17], off nt
	v_lshl_add_u64 v[16:17], v[16:17], 0, s[46:47]
	global_load_dword v116, v[16:17], off nt
	v_lshl_add_u64 v[16:17], v[16:17], 0, s[46:47]
	global_load_dword v107, v[16:17], off nt
	v_lshl_add_u64 v[16:17], v[16:17], 0, s[46:47]
	global_load_dword v117, v[16:17], off nt
	v_lshl_add_u64 v[16:17], v[16:17], 0, s[46:47]
	global_load_dword v108, v[16:17], off nt
	v_lshl_add_u64 v[16:17], v[16:17], 0, s[46:47]
	global_load_dword v118, v[16:17], off nt
	v_lshl_add_u64 v[16:17], v[16:17], 0, s[46:47]
	global_load_dword v109, v[16:17], off nt
	v_lshl_add_u64 v[16:17], v[16:17], 0, s[46:47]
	global_load_dword v119, v[16:17], off nt
	v_lshl_add_u64 v[16:17], v[16:17], 0, s[46:47]
	global_load_dword v110, v[16:17], off nt
	v_lshl_add_u64 v[16:17], v[16:17], 0, s[46:47]
	global_load_dword v120, v[16:17], off nt
	v_lshl_add_u64 v[16:17], v[16:17], 0, s[46:47]
	global_load_dword v111, v[16:17], off nt
	v_lshl_add_u64 v[16:17], v[16:17], 0, s[46:47]
	global_load_dword v121, v[16:17], off nt
	v_lshl_add_u64 v[16:17], v[16:17], 0, s[46:47]
	global_load_dword v112, v[16:17], off nt
	v_lshl_add_u64 v[16:17], v[16:17], 0, s[46:47]
	global_load_dword v122, v[16:17], off nt
	v_lshl_add_u64 v[16:17], v[16:17], 0, s[46:47]
	global_load_dword v102, v[16:17], off nt
	v_lshl_add_u64 v[16:17], v[16:17], 0, s[46:47]
	global_load_dword v103, v[16:17], off nt
	v_lshl_add_u64 v[16:17], v[16:17], 0, s[46:47]
	global_load_dword v113, v[16:17], off nt
	v_lshl_add_u64 v[16:17], v[16:17], 0, s[46:47]
	global_load_dword v123, v[16:17], off nt
	v_lshl_add_u64 v[16:17], v[16:17], 0, s[46:47]
	global_load_dword v125, v[16:17], off nt
	v_lshl_add_u64 v[16:17], v[16:17], 0, s[46:47]
	global_load_dword v126, v[16:17], off nt
	v_lshl_add_u64 v[16:17], v[16:17], 0, s[46:47]
	global_load_dword v127, v[16:17], off nt
	v_lshl_add_u64 v[16:17], v[16:17], 0, s[46:47]
	global_load_dword v128, v[16:17], off nt
	v_lshl_add_u64 v[16:17], v[16:17], 0, s[46:47]
	global_load_dword v129, v[16:17], off nt
	v_lshl_add_u64 v[16:17], v[16:17], 0, s[46:47]
	global_load_dword v130, v[16:17], off nt
	v_lshl_add_u64 v[16:17], v[16:17], 0, s[46:47]
	global_load_dword v131, v[16:17], off nt
	v_lshl_add_u64 v[16:17], v[16:17], 0, s[46:47]
	global_load_dword v132, v[16:17], off nt
	v_lshl_add_u64 v[16:17], v[16:17], 0, s[46:47]
	global_load_dword v133, v[16:17], off nt
	v_lshl_add_u64 v[16:17], v[16:17], 0, s[46:47]
	global_load_dword v134, v[16:17], off nt
	v_lshl_add_u64 v[16:17], v[16:17], 0, s[46:47]
	global_load_dword v135, v[16:17], off nt
	v_lshl_add_u64 v[16:17], v[16:17], 0, s[46:47]
	global_load_dword v136, v[16:17], off nt
	v_lshl_add_u64 v[16:17], v[16:17], 0, s[46:47]
	global_load_dword v137, v[16:17], off nt
	v_lshl_add_u64 v[16:17], v[16:17], 0, s[46:47]
	global_load_dword v138, v[16:17], off nt
	v_lshl_add_u64 v[16:17], v[16:17], 0, s[46:47]
	global_load_dword v139, v[16:17], off nt
	v_lshl_add_u64 v[16:17], v[16:17], 0, s[46:47]
	global_load_dword v140, v[16:17], off nt
	v_lshl_add_u64 v[16:17], v[16:17], 0, s[46:47]
	global_load_dword v141, v[16:17], off nt
	v_lshl_add_u64 v[16:17], v[16:17], 0, s[46:47]
	global_load_dword v142, v[16:17], off nt
	v_lshl_add_u64 v[16:17], v[16:17], 0, s[46:47]
	global_load_dword v143, v[16:17], off nt
	v_lshl_add_u64 v[16:17], v[16:17], 0, s[46:47]
	global_load_dword v144, v[16:17], off nt
	v_lshl_add_u64 v[16:17], v[16:17], 0, s[46:47]
	global_load_dword v146, v[16:17], off nt
	v_lshl_add_u64 v[16:17], v[16:17], 0, s[46:47]
	global_load_dword v147, v[16:17], off nt
	v_lshl_add_u64 v[16:17], v[16:17], 0, s[46:47]
	global_load_dword v148, v[16:17], off nt
	v_lshl_add_u64 v[16:17], v[16:17], 0, s[46:47]
	global_load_dword v149, v[16:17], off nt
	v_lshl_add_u64 v[16:17], v[16:17], 0, s[46:47]
	global_load_dword v151, v[16:17], off nt
	v_lshl_add_u64 v[16:17], v[16:17], 0, s[46:47]
	global_load_dword v152, v[16:17], off nt
	v_lshl_add_u64 v[16:17], v[16:17], 0, s[46:47]
	global_load_dword v153, v[16:17], off nt
	v_lshl_add_u64 v[16:17], v[16:17], 0, s[46:47]
	global_load_dword v154, v[16:17], off nt
	v_lshl_add_u64 v[16:17], v[16:17], 0, s[46:47]
	global_load_dword v155, v[16:17], off nt
	v_lshl_add_u64 v[16:17], v[16:17], 0, s[46:47]
	global_load_dword v157, v[16:17], off nt
	v_lshl_add_u64 v[16:17], v[16:17], 0, s[46:47]
	global_load_dword v158, v[16:17], off nt
	v_lshl_add_u64 v[16:17], v[16:17], 0, s[46:47]
	s_mov_b64 exec, s[100:101]
	global_store_dwordx4 v[172:173], v[180:183], off sc0 sc1 nt
	global_store_dwordx4 v[174:175], v[184:187], off sc0 sc1 nt
	global_store_dwordx4 v[176:177], v[188:191], off sc0 sc1 nt
	global_store_dwordx4 v[178:179], v[192:195], off sc0 sc1 nt
	s_mov_b64 exec, -1
	s_waitcnt vmcnt(63)
	ds_write2st64_b32 v28, v87, v92 offset1:1
	ds_write2st64_b32 v28, v91, v90 offset0:2 offset1:3
	ds_write2st64_b32 v28, v89, v88 offset0:4 offset1:5
	ds_write2st64_b32 v28, v86, v85 offset0:6 offset1:7
	ds_write2st64_b32 v21, v83, v84 offset0:8 offset1:9
	ds_write2st64_b32 v21, v79, v80 offset0:10 offset1:11
	ds_write2st64_b32 v21, v75, v76 offset0:12 offset1:13
	ds_write2st64_b32 v21, v71, v72 offset0:14 offset1:15
	ds_write2st64_b32 v22, v65, v66 offset0:16 offset1:17
	ds_write2st64_b32 v22, v61, v62 offset0:18 offset1:19
	ds_write2st64_b32 v22, v57, v58 offset0:20 offset1:21
	ds_write2st64_b32 v22, v53, v54 offset0:22 offset1:23
	ds_write2st64_b32 v23, v45, v46 offset0:24 offset1:25
	ds_write2st64_b32 v23, v35, v36 offset0:26 offset1:27
	ds_write2st64_b32 v23, v33, v34 offset0:28 offset1:29
	ds_write2st64_b32 v23, v31, v32 offset0:30 offset1:31
	ds_write2st64_b32 v24, v29, v30 offset0:32 offset1:33
	ds_write2st64_b32 v24, v81, v82 offset0:34 offset1:35
	ds_write2st64_b32 v24, v77, v78 offset0:36 offset1:37
	ds_write2st64_b32 v24, v73, v74 offset0:38 offset1:39
	ds_write2st64_b32 v25, v69, v70 offset0:40 offset1:41
	ds_write2st64_b32 v25, v67, v68 offset0:42 offset1:43
	ds_write2st64_b32 v25, v63, v64 offset0:44 offset1:45
	ds_write2st64_b32 v25, v59, v60 offset0:46 offset1:47
	ds_write2st64_b32 v26, v55, v56 offset0:48 offset1:49
	ds_write2st64_b32 v26, v51, v52 offset0:50 offset1:51
	global_load_dword v159, v[16:17], off nt
	ds_write2st64_b32 v26, v38, v39 offset0:52 offset1:53
	ds_write2st64_b32 v26, v40, v42 offset0:54 offset1:55
	ds_write2st64_b32 v27, v37, v41 offset0:56 offset1:57
	ds_write2st64_b32 v27, v43, v44 offset0:58 offset1:59
	ds_write2st64_b32 v27, v47, v48 offset0:60 offset1:61
	ds_write2st64_b32 v27, v49, v50 offset0:62 offset1:63
	s_waitcnt lgkmcnt(0)
	ds_read2_b32 v[16:17], v1 offset1:32
	v_mov_b32_e32 v30, 0
	ds_read2_b32 v[32:33], v1 offset0:128 offset1:160
	v_mov_b32_e32 v31, 0
	v_add_u32_e32 v145, 0x400, v1
	s_waitcnt lgkmcnt(1)
	v_mul_f32_e32 v4, 0x42800000, v16
	v_mul_f32_e32 v15, 0x42800000, v17
	ds_read2_b32 v[16:17], v1 offset0:64 offset1:96
	v_cvt_pk_fp8_f32 v30, v4, v15
	ds_read2_b32 v[34:35], v145 offset0:128 offset1:160
	v_add_u32_e32 v150, 0x400, v9
	ds_read2_b32 v[38:39], v150 offset0:128 offset1:160
	s_waitcnt lgkmcnt(2)
	v_mul_f32_e32 v4, 0x42800000, v16
	v_mul_f32_e32 v15, 0x42800000, v17
	ds_read2_b32 v[16:17], v1 offset0:192 offset1:224
	v_cvt_pk_fp8_f32 v30, v4, v15 op_sel:[0,0,1]
	v_mul_f32_e32 v4, 0x42800000, v32
	v_mul_f32_e32 v15, 0x42800000, v33
	v_cvt_pk_fp8_f32 v31, v4, v15
	s_waitcnt lgkmcnt(0)
	v_mul_f32_e32 v4, 0x42800000, v16
	v_mul_f32_e32 v15, 0x42800000, v17
	ds_read2_b32 v[16:17], v145 offset0:64 offset1:96
	ds_read2_b32 v[32:33], v145 offset1:32
	v_cvt_pk_fp8_f32 v31, v4, v15 op_sel:[0,0,1]
	v_lshl_add_u64 v[10:11], v[10:11], 0, v[6:7]
	v_add_u32_e32 v156, 0x400, v18
	s_waitcnt lgkmcnt(1)
	v_mul_f32_e32 v29, 0x42800000, v16
	v_mul_f32_e32 v36, 0x42800000, v17
	ds_read2_b32 v[16:17], v145 offset0:192 offset1:224
	s_waitcnt lgkmcnt(1)
	v_mul_f32_e32 v4, 0x42800000, v32
	v_mul_f32_e32 v15, 0x42800000, v33
	v_mov_b32_e32 v32, 0
	v_cvt_pk_fp8_f32 v32, v4, v15
	v_mul_f32_e32 v4, 0x42800000, v34
	v_mul_f32_e32 v15, 0x42800000, v35
	v_mov_b32_e32 v33, 0
	ds_read2_b32 v[34:35], v9 offset1:32
	v_cvt_pk_fp8_f32 v33, v4, v15
	s_waitcnt lgkmcnt(1)
	v_mul_f32_e32 v4, 0x42800000, v16
	v_mul_f32_e32 v15, 0x42800000, v17
	ds_read2_b32 v[16:17], v9 offset0:64 offset1:96
	v_cvt_pk_fp8_f32 v32, v29, v36 op_sel:[0,0,1]
	ds_read2_b32 v[36:37], v9 offset0:128 offset1:160
	v_cvt_pk_fp8_f32 v33, v4, v15 op_sel:[0,0,1]
	s_waitcnt lgkmcnt(2)
	v_mul_f32_e32 v4, 0x42800000, v34
	v_mul_f32_e32 v15, 0x42800000, v35
	v_mov_b32_e32 v34, 0
	v_cvt_pk_fp8_f32 v34, v4, v15
	s_waitcnt lgkmcnt(1)
	v_mul_f32_e32 v4, 0x42800000, v16
	v_mul_f32_e32 v15, 0x42800000, v17
	ds_read2_b32 v[16:17], v9 offset0:192 offset1:224
	s_waitcnt lgkmcnt(1)
	v_mul_f32_e32 v29, 0x42800000, v36
	v_mul_f32_e32 v36, 0x42800000, v37
	v_mov_b32_e32 v35, 0
	v_cvt_pk_fp8_f32 v35, v29, v36
	ds_read2_b32 v[36:37], v150 offset1:32
	v_cvt_pk_fp8_f32 v34, v4, v15 op_sel:[0,0,1]
	s_waitcnt lgkmcnt(1)
	v_mul_f32_e32 v4, 0x42800000, v16
	v_mul_f32_e32 v15, 0x42800000, v17
	ds_read2_b32 v[16:17], v150 offset0:64 offset1:96
	v_cvt_pk_fp8_f32 v35, v4, v15 op_sel:[0,0,1]
	s_waitcnt lgkmcnt(1)
	v_mul_f32_e32 v4, 0x42800000, v36
	v_mul_f32_e32 v15, 0x42800000, v37
	v_mov_b32_e32 v36, 0
	v_cvt_pk_fp8_f32 v36, v4, v15
	s_waitcnt lgkmcnt(0)
	v_mul_f32_e32 v4, 0x42800000, v16
	v_mul_f32_e32 v15, 0x42800000, v17
	ds_read2_b32 v[16:17], v150 offset0:192 offset1:224
	v_cvt_pk_fp8_f32 v36, v4, v15 op_sel:[0,0,1]
	v_mul_f32_e32 v4, 0x42800000, v38
	v_mul_f32_e32 v15, 0x42800000, v39
	v_mov_b32_e32 v37, 0
	v_cvt_pk_fp8_f32 v37, v4, v15
	s_waitcnt lgkmcnt(0)
; __device__ __forceinline__ MoeItem moe_item(const float* wg, const float* wu, const float* wd, const float* win, const float* wout, const float* wpn, const float* wpd, unsigned char* ws, int r, int lane) {
;     if (r >= NMOE_X + NGATE_IT + NWO_IT) { const int q = r - NMOE_X - NGATE_IT - NWO_IT, which = q >> 9, kb = (q >> 6) & 7, nb = q & 63; MoeItem it; it.stride = DM; it.dpitch = 1024;
;         it.src = (which ? wpd : wpn) + (size_t)(kb * 128 + (lane >> 5)) * DM + nb * 32 + (lane & 31);
;         it.dst = ws + (which ? WS_WPDFT : WS_WPNAT) + (size_t)(nb * 32) * 1024 + kb * 128 + (size_t)(lane >> 3) * 1024 + 16 * (lane & 7); return it; }
;     if (r >= NMOE_X + NGATE_IT) { const int q = r - NMOE_X - NGATE_IT, kb = q >> 6, nb = q & 63; MoeItem it; it.stride = DM; it.dpitch = DM;
;         it.src = wout + (size_t)(kb * 128 + (lane >> 5)) * DM + nb * 32 + (lane & 31);
;         it.dst = ws + WS_WO8 + (size_t)(nb * 32) * DM + kb * 128 + (size_t)(lane >> 3) * DM + 16 * (lane & 7); return it; }
;     if (r >= NMOE_X) { const int q = r - NMOE_X, kb = q / 192, nb = q % 192; MoeItem it; it.stride = INC; it.dpitch = DM;
;         const int scol = nb < 128 ? 6144 + nb * 32 : (nb < 160 ? 1024 + (nb - 128) * 32 : 3072 + (nb - 160) * 32);
;         it.src = win + (size_t)(kb * 128 + (lane >> 5)) * INC + scol + (lane & 31);
;         it.dst = ws + WS_WG8 + (size_t)(nb * 32) * DM + kb * 128 + (size_t)(lane >> 3) * DM + 16 * (lane & 7); return it; }
;     const int mat = r / MOE_IE, q = r % MOE_IE, e = mat / 3, which = mat % 3, kb = q / 64, nb = q % 64, n0 = nb * 32;
;     const float* src = (which == 0 ? wg : (which == 1 ? wu : wd)) + (size_t)e * DM * DFF + (size_t)(kb * 128 + (lane >> 5)) * DFF + n0 + (lane & 31);
;     unsigned char* dst;
;     if (which < 2) dst = ws + WS_WGUT + ((size_t)(e * 16 + (n0 >> 7)) * 256 + which * 128 + (n0 & 127)) * DM;
;     else dst = ws + WS_WDT + ((size_t)e * DM + n0) * DFF;
;     MoeItem it; it.stride = DFF; it.dpitch = DM; it.src = src; it.dst = dst + kb * 128 + (size_t)(lane >> 3) * DM + 16 * (lane & 7); return it;
	v_mul_f32_e32 v4, 0x42800000, v16
	v_mul_f32_e32 v15, 0x42800000, v17
	ds_read2_b32 v[16:17], v18 offset1:32
	v_cvt_pk_fp8_f32 v37, v4, v15 op_sel:[0,0,1]
	s_nop 0
	v_mov_b64_e32 v[196:197], v[10:11]
	v_mov_b64_e32 v[204:205], v[30:31]
	v_mov_b64_e32 v[206:207], v[32:33]
	ds_read2_b32 v[32:33], v18 offset0:64 offset1:96
	s_lshl_b64 s[38:39], s[38:39], 3
	s_waitcnt lgkmcnt(1)
	v_mul_f32_e32 v4, 0x42800000, v16
	v_mul_f32_e32 v15, 0x42800000, v17
	ds_read2_b32 v[16:17], v18 offset0:128 offset1:160
	v_mov_b32_e32 v30, 0
	v_cvt_pk_fp8_f32 v30, v4, v15
	s_waitcnt lgkmcnt(1)
	v_mul_f32_e32 v4, 0x42800000, v32
	v_mov_b32_e32 v31, 0
	s_waitcnt lgkmcnt(0)
	v_mul_f32_e32 v29, 0x42800000, v16
	v_mul_f32_e32 v32, 0x42800000, v17
	ds_read2_b32 v[16:17], v18 offset0:192 offset1:224
	v_mul_f32_e32 v15, 0x42800000, v33
	v_cvt_pk_fp8_f32 v31, v29, v32
	ds_read2_b32 v[32:33], v156 offset1:32
	v_cvt_pk_fp8_f32 v30, v4, v15 op_sel:[0,0,1]
	s_waitcnt lgkmcnt(1)
	v_mul_f32_e32 v4, 0x42800000, v16
	v_mul_f32_e32 v15, 0x42800000, v17
	ds_read2_b32 v[16:17], v156 offset0:64 offset1:96
	v_lshl_add_u64 v[10:11], v[10:11], 0, s[38:39]
	s_nop 0
	v_mov_b64_e32 v[198:199], v[10:11]
	v_mov_b64_e32 v[208:209], v[34:35]
	v_mov_b64_e32 v[210:211], v[36:37]
	ds_read2_b32 v[34:35], v156 offset0:128 offset1:160
	v_cvt_pk_fp8_f32 v31, v4, v15 op_sel:[0,0,1]
	s_waitcnt lgkmcnt(2)
	v_mul_f32_e32 v4, 0x42800000, v32
	v_mul_f32_e32 v15, 0x42800000, v33
	v_mov_b32_e32 v32, 0
	v_cvt_pk_fp8_f32 v32, v4, v15
	s_waitcnt lgkmcnt(1)
	v_mul_f32_e32 v4, 0x42800000, v16
	v_mul_f32_e32 v15, 0x42800000, v17
	ds_read2_b32 v[16:17], v156 offset0:192 offset1:224
	s_waitcnt lgkmcnt(1)
	v_mul_f32_e32 v29, 0x42800000, v34
	v_mul_f32_e32 v34, 0x42800000, v35
	v_mov_b32_e32 v33, 0
	v_cvt_pk_fp8_f32 v33, v29, v34
	ds_read2_b32 v[34:35], v19 offset1:32
	v_cvt_pk_fp8_f32 v32, v4, v15 op_sel:[0,0,1]
	s_waitcnt lgkmcnt(1)
	v_mul_f32_e32 v4, 0x42800000, v16
	v_mul_f32_e32 v15, 0x42800000, v17
	ds_read2_b32 v[16:17], v19 offset0:64 offset1:96
	ds_read2_b32 v[36:37], v19 offset0:128 offset1:160
	v_cvt_pk_fp8_f32 v33, v4, v15 op_sel:[0,0,1]
	s_waitcnt lgkmcnt(2)
	v_mul_f32_e32 v4, 0x42800000, v34
	v_mul_f32_e32 v15, 0x42800000, v35
	v_mov_b32_e32 v34, 0
	v_cvt_pk_fp8_f32 v34, v4, v15
	s_waitcnt lgkmcnt(1)
	v_mul_f32_e32 v4, 0x42800000, v16
	v_mul_f32_e32 v15, 0x42800000, v17
	ds_read2_b32 v[16:17], v19 offset0:192 offset1:224
	s_waitcnt lgkmcnt(1)
	v_mul_f32_e32 v29, 0x42800000, v36
	v_mul_f32_e32 v36, 0x42800000, v37
	v_mov_b32_e32 v35, 0
	v_add_u32_e32 v160, 0x400, v19
	v_cvt_pk_fp8_f32 v35, v29, v36
	ds_read2_b32 v[36:37], v160 offset1:32
	v_cvt_pk_fp8_f32 v34, v4, v15 op_sel:[0,0,1]
	s_waitcnt lgkmcnt(1)
	v_mul_f32_e32 v4, 0x42800000, v16
	v_mul_f32_e32 v15, 0x42800000, v17
	ds_read2_b32 v[16:17], v160 offset0:64 offset1:96
	ds_read2_b32 v[38:39], v160 offset0:128 offset1:160
	v_cvt_pk_fp8_f32 v35, v4, v15 op_sel:[0,0,1]
	s_waitcnt lgkmcnt(2)
	v_mul_f32_e32 v4, 0x42800000, v36
	v_mul_f32_e32 v15, 0x42800000, v37
	v_mov_b32_e32 v36, 0
	v_cvt_pk_fp8_f32 v36, v4, v15
	s_waitcnt lgkmcnt(1)
	v_mul_f32_e32 v4, 0x42800000, v16
	v_mul_f32_e32 v15, 0x42800000, v17
	ds_read2_b32 v[16:17], v160 offset0:192 offset1:224
	s_waitcnt lgkmcnt(1)
	v_mul_f32_e32 v29, 0x42800000, v38
	v_mul_f32_e32 v38, 0x42800000, v39
	v_mov_b32_e32 v37, 0
	v_cvt_pk_fp8_f32 v37, v29, v38
	v_cvt_pk_fp8_f32 v36, v4, v15 op_sel:[0,0,1]
	s_waitcnt lgkmcnt(0)
	v_mul_f32_e32 v4, 0x42800000, v16
	v_mul_f32_e32 v15, 0x42800000, v17
	v_cvt_pk_fp8_f32 v37, v4, v15 op_sel:[0,0,1]
	v_lshl_add_u64 v[10:11], v[10:11], 0, s[38:39]
	s_nop 0
	v_mov_b64_e32 v[200:201], v[10:11]
	v_mov_b64_e32 v[212:213], v[30:31]
	v_mov_b64_e32 v[214:215], v[32:33]
	v_lshl_add_u64 v[10:11], v[10:11], 0, s[38:39]
	s_nop 0
	v_mov_b64_e32 v[202:203], v[10:11]
	v_mov_b64_e32 v[216:217], v[34:35]
	v_mov_b64_e32 v[218:219], v[36:37]
	s_waitcnt lgkmcnt(0)
	s_add_i32 s3, s89, s3
	s_mov_b32 s96, 0
	s_min_i32 s43, s3, s7
	s_cmp_lt_i32 s43, 0x19000
	s_mov_b64 s[38:39], -1
	s_cbranch_scc0 .LBB0_126
	s_cmp_lt_i32 s43, 0x18c00
	s_cbranch_scc0 .LBB0_123
	s_cmp_lt_i32 s43, 0x18000
	s_cbranch_scc0 .LBB0_113
	s_mov_b32 s96, 1
	s_ashr_i32 s4, s43, 31
	s_lshr_b32 s4, s4, 22
	s_add_i32 s4, s43, s4
	s_ashr_i32 s39, s4, 10
	s_and_b32 s4, s4, 0xfc00
	s_sub_i32 s46, s43, s4
	s_mul_hi_i32 s4, s43, 0x2aaaaaab
	s_lshr_b32 s38, s4, 31
	s_ashr_i32 s4, s4, 9
	s_add_i32 s38, s4, s38
	s_mul_hi_i32 s4, s39, 0x55555556
	s_lshr_b32 s45, s4, 31
	s_add_i32 s4, s4, s45
	s_mul_i32 s4, s4, 3
	s_sub_i32 s4, s39, s4
	s_sext_i32_i16 s39, s46
	s_bfe_u32 s39, s39, 0x60019
	s_add_i32 s45, s46, s39
	s_and_b32 s39, s45, 0xffc0
	s_sub_i32 s39, s46, s39
	s_sext_i32_i16 s84, s39
	s_lshl_b32 s46, s84, 5
	s_ashr_i32 s39, s38, 31
	s_ashr_i32 s47, s46, 31
	s_cmp_gt_i32 s4, 1
	s_mov_b64 s[70:71], -1
	s_cbranch_scc0 .LBB0_110
	s_lshl_b64 s[68:69], s[38:39], 22
	s_lshl_b64 s[70:71], s[46:47], 11
	s_add_u32 s68, s73, s68
	s_addc_u32 s69, s74, s69
	s_add_u32 s68, s68, s70
	s_addc_u32 s69, s69, s71
	s_mov_b64 s[70:71], 0

; __device__ __forceinline__ unsigned f2bf(float f) { unsigned u = __float_as_uint(f); return (u + 0x7fffu + ((u >> 16) & 1u)) >> 16; }
;     ...
;     if (parts & 4) for (int i = gt; i < 32 * 2048; i += NGT) { const int e = i >> 11, k = i & 2047; const float w = F.in[I_WR][k * 32 + e]; const unsigned hb = f2bf(w); const float lo = w - __uint_as_float(hb << 16);
;         ((bf16_t*)(F.ws + WS_WRT))[i] = (bf16_t)hb; ((bf16_t*)(F.ws + WS_WRT))[65536 + i] = (bf16_t)f2bf(lo); }
.LBB0_130:
	s_mov_b64 exec, s[100:101]
	global_store_dwordx4 v[172:173], v[180:183], off sc0 sc1 nt
	global_store_dwordx4 v[174:175], v[184:187], off sc0 sc1 nt
	global_store_dwordx4 v[176:177], v[188:191], off sc0 sc1 nt
	global_store_dwordx4 v[178:179], v[192:195], off sc0 sc1 nt
	s_mov_b64 exec, -1
	v_readlane_b32 s3, v255, 2
	s_nop 1
	v_lshl_or_b32 v2, s3, 9, v0
	s_mov_b32 s3, 0x10000
	v_cmp_gt_i32_e32 vcc, s3, v2
	v_ashrrev_i32_e32 v3, 31, v2
	s_and_saveexec_b64 s[4:5], vcc
	s_cbranch_execz .LBB0_133
	s_lshl_b32 s16, s33, 9
	v_lshl_add_u64 v[4:5], v[2:3], 1, s[82:83]
	s_mov_b64 s[6:7], 0x3c00000
	s_ashr_i32 s17, s16, 31
	v_lshlrev_b32_e32 v1, 5, v0
	v_readlane_b32 s3, v255, 2
	v_lshl_add_u64 v[4:5], v[4:5], 0, s[6:7]
	s_lshl_b64 s[20:21], s[16:17], 1
	v_lshl_or_b32 v1, s3, 14, v1
	s_lshl_b32 s3, s33, 14
	s_mov_b64 s[24:25], 0
	s_movk_i32 s6, 0x7fff
	s_mov_b32 s7, 0xffff
	v_mov_b32_e32 v6, v2
